# router L0+L1 deferred unpack + hoisted bias; conv L1 wait moved after store
# speedup vs baseline: 1.0018x; 1.0018x over previous
.LBB0_1043:
	s_or_b64 exec, exec, s[8:9]
	s_add_u32 s40, s34, 0xd00000
	s_addc_u32 s41, s35, 0
	s_add_u32 s42, s34, 0xe80000
	s_addc_u32 s43, s35, 0
	s_sub_i32 s66, s56, s23
	s_and_saveexec_b64 s[44:45], s[2:3]
	s_cbranch_execz .LBB0_1090
	s_waitcnt vmcnt(62)
	v_cvt_pk_bf16_f32 v0, v4, v5
	v_lshlrev_b32_e32 v100, 16, v0
	v_and_b32_e32 v101, 0xffff0000, v0
	s_waitcnt vmcnt(60)
	v_cvt_pk_bf16_f32 v1, v2, v3
	v_pk_add_f32 v[4:5], v[4:5], v[100:101] neg_lo:[0,1] neg_hi:[0,1]
	v_lshlrev_b32_e32 v100, 16, v1
	v_and_b32_e32 v101, 0xffff0000, v1
	v_pk_add_f32 v[2:3], v[2:3], v[100:101] neg_lo:[0,1] neg_hi:[0,1]
	v_cvt_pk_bf16_f32 v4, v4, v5
	v_cvt_pk_bf16_f32 v5, v2, v3
	s_waitcnt vmcnt(54)
	v_cvt_pk_bf16_f32 v2, v6, v7
	v_lshlrev_b32_e32 v100, 16, v2
	v_and_b32_e32 v101, 0xffff0000, v2
	s_waitcnt vmcnt(52)
	v_cvt_pk_bf16_f32 v3, v8, v9
	v_pk_add_f32 v[6:7], v[6:7], v[100:101] neg_lo:[0,1] neg_hi:[0,1]
	v_lshlrev_b32_e32 v100, 16, v3
	v_and_b32_e32 v101, 0xffff0000, v3
	v_pk_add_f32 v[8:9], v[8:9], v[100:101] neg_lo:[0,1] neg_hi:[0,1]
	v_cvt_pk_bf16_f32 v6, v6, v7
	v_cvt_pk_bf16_f32 v7, v8, v9
	s_waitcnt vmcnt(46)
	v_cvt_pk_bf16_f32 v8, v12, v13
	v_lshlrev_b32_e32 v100, 16, v8
	v_and_b32_e32 v101, 0xffff0000, v8
	s_waitcnt vmcnt(44)
	v_cvt_pk_bf16_f32 v9, v10, v11
	v_pk_add_f32 v[12:13], v[12:13], v[100:101] neg_lo:[0,1] neg_hi:[0,1]
	v_lshlrev_b32_e32 v100, 16, v9
	v_and_b32_e32 v101, 0xffff0000, v9
	v_pk_add_f32 v[10:11], v[10:11], v[100:101] neg_lo:[0,1] neg_hi:[0,1]
	v_cvt_pk_bf16_f32 v12, v12, v13
	v_cvt_pk_bf16_f32 v13, v10, v11
	s_waitcnt vmcnt(38)
	v_cvt_pk_bf16_f32 v10, v14, v15
	v_lshlrev_b32_e32 v100, 16, v10
	v_and_b32_e32 v101, 0xffff0000, v10
	s_waitcnt vmcnt(36)
	v_cvt_pk_bf16_f32 v11, v16, v17
	v_pk_add_f32 v[14:15], v[14:15], v[100:101] neg_lo:[0,1] neg_hi:[0,1]
	v_lshlrev_b32_e32 v100, 16, v11
	v_and_b32_e32 v101, 0xffff0000, v11
	v_pk_add_f32 v[16:17], v[16:17], v[100:101] neg_lo:[0,1] neg_hi:[0,1]
	v_cvt_pk_bf16_f32 v14, v14, v15
	v_cvt_pk_bf16_f32 v15, v16, v17
	s_waitcnt vmcnt(30)
	v_cvt_pk_bf16_f32 v16, v20, v21
	v_lshlrev_b32_e32 v100, 16, v16
	v_and_b32_e32 v101, 0xffff0000, v16
	s_waitcnt vmcnt(28)
	v_cvt_pk_bf16_f32 v17, v18, v19
	v_pk_add_f32 v[20:21], v[20:21], v[100:101] neg_lo:[0,1] neg_hi:[0,1]
	v_lshlrev_b32_e32 v100, 16, v17
	v_and_b32_e32 v101, 0xffff0000, v17
	v_pk_add_f32 v[18:19], v[18:19], v[100:101] neg_lo:[0,1] neg_hi:[0,1]
	v_cvt_pk_bf16_f32 v20, v20, v21
	v_cvt_pk_bf16_f32 v21, v18, v19
	s_waitcnt vmcnt(22)
	v_cvt_pk_bf16_f32 v18, v22, v23
	v_lshlrev_b32_e32 v100, 16, v18
	v_and_b32_e32 v101, 0xffff0000, v18
	s_waitcnt vmcnt(20)
	v_cvt_pk_bf16_f32 v19, v24, v25
	v_pk_add_f32 v[22:23], v[22:23], v[100:101] neg_lo:[0,1] neg_hi:[0,1]
	v_lshlrev_b32_e32 v100, 16, v19
	v_and_b32_e32 v101, 0xffff0000, v19
	v_pk_add_f32 v[24:25], v[24:25], v[100:101] neg_lo:[0,1] neg_hi:[0,1]
	v_cvt_pk_bf16_f32 v22, v22, v23
	v_cvt_pk_bf16_f32 v23, v24, v25
	s_waitcnt vmcnt(14)
	v_cvt_pk_bf16_f32 v24, v28, v29
	v_lshlrev_b32_e32 v100, 16, v24
	v_and_b32_e32 v101, 0xffff0000, v24
	s_waitcnt vmcnt(12)
	v_cvt_pk_bf16_f32 v25, v26, v27
	v_pk_add_f32 v[28:29], v[28:29], v[100:101] neg_lo:[0,1] neg_hi:[0,1]
	v_lshlrev_b32_e32 v100, 16, v25
	v_and_b32_e32 v101, 0xffff0000, v25
	v_pk_add_f32 v[26:27], v[26:27], v[100:101] neg_lo:[0,1] neg_hi:[0,1]
	v_cvt_pk_bf16_f32 v28, v28, v29
	v_cvt_pk_bf16_f32 v29, v26, v27
	s_waitcnt vmcnt(6)
	v_cvt_pk_bf16_f32 v26, v30, v31
	v_lshlrev_b32_e32 v100, 16, v26
	v_and_b32_e32 v101, 0xffff0000, v26
	s_waitcnt vmcnt(4)
	v_cvt_pk_bf16_f32 v27, v32, v33
	v_pk_add_f32 v[30:31], v[30:31], v[100:101] neg_lo:[0,1] neg_hi:[0,1]
	v_lshlrev_b32_e32 v100, 16, v27
	v_and_b32_e32 v101, 0xffff0000, v27
	v_pk_add_f32 v[32:33], v[32:33], v[100:101] neg_lo:[0,1] neg_hi:[0,1]
	v_cvt_pk_bf16_f32 v30, v30, v31
	v_cvt_pk_bf16_f32 v31, v32, v33
	v_cvt_pk_bf16_f32 v32, v36, v37
	v_lshlrev_b32_e32 v100, 16, v32
	v_and_b32_e32 v101, 0xffff0000, v32
	v_cvt_pk_bf16_f32 v33, v34, v35
	v_pk_add_f32 v[36:37], v[36:37], v[100:101] neg_lo:[0,1] neg_hi:[0,1]
	v_lshlrev_b32_e32 v100, 16, v33
	v_and_b32_e32 v101, 0xffff0000, v33
	v_pk_add_f32 v[34:35], v[34:35], v[100:101] neg_lo:[0,1] neg_hi:[0,1]
	v_cvt_pk_bf16_f32 v36, v36, v37
	v_cvt_pk_bf16_f32 v37, v34, v35
	v_cvt_pk_bf16_f32 v34, v38, v39
	v_lshlrev_b32_e32 v100, 16, v34
	v_and_b32_e32 v101, 0xffff0000, v34
	v_cvt_pk_bf16_f32 v35, v40, v41
	v_pk_add_f32 v[38:39], v[38:39], v[100:101] neg_lo:[0,1] neg_hi:[0,1]
	v_lshlrev_b32_e32 v100, 16, v35
	v_and_b32_e32 v101, 0xffff0000, v35
	v_pk_add_f32 v[40:41], v[40:41], v[100:101] neg_lo:[0,1] neg_hi:[0,1]
	v_cvt_pk_bf16_f32 v38, v38, v39
	v_cvt_pk_bf16_f32 v39, v40, v41
	v_cvt_pk_bf16_f32 v40, v44, v45
	v_lshlrev_b32_e32 v100, 16, v40
	v_and_b32_e32 v101, 0xffff0000, v40
	v_cvt_pk_bf16_f32 v41, v42, v43
	v_pk_add_f32 v[44:45], v[44:45], v[100:101] neg_lo:[0,1] neg_hi:[0,1]
	v_lshlrev_b32_e32 v100, 16, v41
	v_and_b32_e32 v101, 0xffff0000, v41
	v_pk_add_f32 v[42:43], v[42:43], v[100:101] neg_lo:[0,1] neg_hi:[0,1]
	v_cvt_pk_bf16_f32 v44, v44, v45
	v_cvt_pk_bf16_f32 v45, v42, v43
	v_cvt_pk_bf16_f32 v42, v46, v47
	v_lshlrev_b32_e32 v100, 16, v42
	v_and_b32_e32 v101, 0xffff0000, v42
	v_cvt_pk_bf16_f32 v43, v48, v49
	v_pk_add_f32 v[46:47], v[46:47], v[100:101] neg_lo:[0,1] neg_hi:[0,1]
	v_lshlrev_b32_e32 v100, 16, v43
	v_and_b32_e32 v101, 0xffff0000, v43
	v_pk_add_f32 v[48:49], v[48:49], v[100:101] neg_lo:[0,1] neg_hi:[0,1]
	v_cvt_pk_bf16_f32 v46, v46, v47
	v_cvt_pk_bf16_f32 v47, v48, v49
	v_cvt_pk_bf16_f32 v48, v52, v53
	v_lshlrev_b32_e32 v100, 16, v48
	v_and_b32_e32 v101, 0xffff0000, v48
	v_cvt_pk_bf16_f32 v49, v50, v51
	v_pk_add_f32 v[52:53], v[52:53], v[100:101] neg_lo:[0,1] neg_hi:[0,1]
	v_lshlrev_b32_e32 v100, 16, v49
	v_and_b32_e32 v101, 0xffff0000, v49
	v_pk_add_f32 v[50:51], v[50:51], v[100:101] neg_lo:[0,1] neg_hi:[0,1]
	v_cvt_pk_bf16_f32 v52, v52, v53
	v_cvt_pk_bf16_f32 v53, v50, v51
	v_cvt_pk_bf16_f32 v50, v54, v55
	v_lshlrev_b32_e32 v100, 16, v50
	v_and_b32_e32 v101, 0xffff0000, v50
	v_cvt_pk_bf16_f32 v51, v56, v57
	v_pk_add_f32 v[54:55], v[54:55], v[100:101] neg_lo:[0,1] neg_hi:[0,1]
	v_lshlrev_b32_e32 v100, 16, v51
	v_and_b32_e32 v101, 0xffff0000, v51
	v_pk_add_f32 v[56:57], v[56:57], v[100:101] neg_lo:[0,1] neg_hi:[0,1]
	v_cvt_pk_bf16_f32 v54, v54, v55
	v_cvt_pk_bf16_f32 v55, v56, v57
	v_cvt_pk_bf16_f32 v56, v60, v61
	v_lshlrev_b32_e32 v100, 16, v56
	v_and_b32_e32 v101, 0xffff0000, v56
	v_cvt_pk_bf16_f32 v57, v58, v59
	v_pk_add_f32 v[60:61], v[60:61], v[100:101] neg_lo:[0,1] neg_hi:[0,1]
	v_lshlrev_b32_e32 v100, 16, v57
	v_and_b32_e32 v101, 0xffff0000, v57
	v_pk_add_f32 v[58:59], v[58:59], v[100:101] neg_lo:[0,1] neg_hi:[0,1]
	v_cvt_pk_bf16_f32 v60, v60, v61
	v_cvt_pk_bf16_f32 v61, v58, v59
	s_waitcnt vmcnt(0)
	v_cvt_pk_bf16_f32 v58, v62, v63
	v_lshlrev_b32_e32 v100, 16, v58
	v_and_b32_e32 v101, 0xffff0000, v58
	v_cvt_pk_bf16_f32 v59, v98, v99
	v_pk_add_f32 v[62:63], v[62:63], v[100:101] neg_lo:[0,1] neg_hi:[0,1]
	v_lshlrev_b32_e32 v100, 16, v59
	v_and_b32_e32 v101, 0xffff0000, v59
	v_pk_add_f32 v[98:99], v[98:99], v[100:101] neg_lo:[0,1] neg_hi:[0,1]
	v_cvt_pk_bf16_f32 v62, v62, v63
	v_cvt_pk_bf16_f32 v63, v98, v99
	v_mov_b32_e32 v99, 0
	s_add_u32 s46, s34, 0xdc0000
	v_mov_b32_e32 v65, v99
	s_addc_u32 s47, s35, 0
	v_lshl_add_u64 v[102:103], s[34:35], 0, v[64:65]
	s_mov_b64 s[8:9], 0x6a600000
	s_add_u32 s48, s34, 0x500000
	v_lshl_add_u64 v[100:101], s[28:29], 0, v[64:65]
	v_lshl_add_u64 v[102:103], v[102:103], 0, s[8:9]
	s_movk_i32 s8, 0x810
	v_lshl_or_b32 v65, s14, 4, v104
	s_movk_i32 s15, 0x84
	s_addc_u32 s49, s35, 0
	v_mad_u32_u24 v111, v104, s8, 0
	v_mul_lo_u32 v65, v65, s15
	s_add_i32 s8, 0, 0x10200
	v_add_u32_e32 v113, s8, v65
	v_and_b32_e32 v65, 31, v146
	v_lshlrev_b32_e32 v98, 2, v65
	v_lshlrev_b32_e32 v108, 2, v105
	v_lshrrev_b32_e32 v106, 5, v105
	v_lshl_add_u64 v[104:105], s[6:7], 0, v[98:99]
	v_add_u32_e32 v116, s8, v98
	v_and_b32_e32 v98, 64, v147
	v_add_u32_e32 v98, 64, v98
	v_xor_b32_e32 v117, 1, v147
	v_cmp_lt_i32_e32 vcc, v117, v98
	s_lshl_b32 s67, s14, 1
	v_and_b32_e32 v107, 48, v146
	v_cndmask_b32_e32 v117, v147, v117, vcc
	v_lshlrev_b32_e32 v137, 2, v117
	v_xor_b32_e32 v117, 2, v147
	v_cmp_lt_i32_e32 vcc, v117, v98
	v_or_b32_e32 v115, s67, v106
	v_lshl_or_b32 v109, s14, 8, v107
	v_cndmask_b32_e32 v117, v147, v117, vcc
	v_lshlrev_b32_e32 v138, 2, v117
	v_xor_b32_e32 v117, 4, v147
	v_cmp_lt_i32_e32 vcc, v117, v98
	s_mul_i32 s50, s14, 0x1020
	v_mul_lo_u32 v115, v115, s15
	v_cndmask_b32_e32 v117, v147, v117, vcc
	v_lshlrev_b32_e32 v139, 2, v117
	v_xor_b32_e32 v117, 8, v147
	v_cmp_lt_i32_e32 vcc, v117, v98
	s_lshl_b32 s15, s22, 8
	s_lshl_b32 s14, s14, 3
	v_cndmask_b32_e32 v117, v147, v117, vcc
	v_lshlrev_b32_e32 v140, 2, v117
	v_xor_b32_e32 v117, 16, v147
	v_cmp_lt_i32_e32 vcc, v117, v98
	s_add_i32 s14, s14, s15
	s_add_i32 s68, s50, 0
	v_cndmask_b32_e32 v117, v147, v117, vcc
	v_lshlrev_b32_e32 v141, 2, v117
	v_xor_b32_e32 v117, 32, v147
	v_cmp_lt_i32_e32 vcc, v117, v98
	s_or_b32 s50, s67, 1
	v_or_b32_e32 v110, 0x100, v108
	v_cndmask_b32_e32 v98, v147, v117, vcc
	v_lshlrev_b32_e32 v142, 2, v98
	v_lshl_add_u32 v98, v144, 6, s14
	v_lshl_or_b32 v98, v106, 2, v98
	s_mov_b32 s14, 0xffff7800
	v_add3_u32 v106, v98, v65, s14
	v_add_lshl_u32 v98, v144, s56, 4
	s_lshl_b32 s14, s22, 3
	v_or_b32_e32 v112, 0x200, v108
	v_or_b32_e32 v114, 0x300, v108
	s_mulk_i32 s50, 0x810
	v_lshl_add_u32 v143, s22, 7, v98
	s_add_i32 s72, s56, s14
	v_lshlrev_b32_e64 v98, 4, s33
	s_lshl_b32 s73, s22, 2
	v_cmp_gt_u32_e64 s[6:7], 4, v65
	v_cmp_eq_u32_e64 s[8:9], 0, v65
	v_cmp_eq_u32_e64 s[10:11], 1, v65
	v_cmp_eq_u32_e64 s[12:13], 2, v65
	s_add_i32 s69, s50, 0
	s_lshl_b32 s70, s66, 6
	s_lshl_b32 s71, s66, 4
	s_addk_i32 s72, 0xfbc0
	v_lshl_add_u32 v144, s22, 6, v98
	s_addk_i32 s73, 0xfde0
	s_mov_b64 s[50:51], 0
	s_mov_b64 s[52:53], 0x3000
	s_mov_b64 s[54:55], 0x4000
	v_mov_b32_e32 v145, 0x358637bd
	s_mov_b32 s74, 0x800000
	v_lshlrev_b32_e32 v98, 2, v108
	v_lshlrev_b32_e32 v108, 2, v110
	v_lshlrev_b32_e32 v110, 2, v112
	v_lshlrev_b32_e32 v112, 2, v114
	v_add_u32_e32 v147, v111, v109
	v_add_u32_e32 v148, v113, v107
	v_add_u32_e32 v149, v116, v115
	v_mov_b32_e32 v150, 1
	v_mov_b32_e32 v151, 0xff61b1e6
	global_load_dword v203, v[104:105], off
	s_branch .LBB0_1046
.LBB0_1045:
	s_or_b64 exec, exec, s[14:15]
	s_waitcnt vmcnt(8)
	v_lshlrev_b32_e32 v66, 16, v68
	v_and_b32_e32 v67, 0xffff0000, v68
	v_lshlrev_b32_e32 v68, 16, v69
	v_and_b32_e32 v69, 0xffff0000, v69
	v_lshlrev_b32_e32 v70, 16, v72
	v_and_b32_e32 v71, 0xffff0000, v72
	v_lshlrev_b32_e32 v72, 16, v73
	v_and_b32_e32 v73, 0xffff0000, v73
	v_lshlrev_b32_e32 v74, 16, v76
	v_and_b32_e32 v75, 0xffff0000, v76
	v_lshlrev_b32_e32 v76, 16, v77
	v_and_b32_e32 v77, 0xffff0000, v77
	v_lshlrev_b32_e32 v78, 16, v80
	v_and_b32_e32 v79, 0xffff0000, v80
	v_lshlrev_b32_e32 v80, 16, v81
	v_and_b32_e32 v81, 0xffff0000, v81
	v_lshlrev_b32_e32 v82, 16, v84
	v_and_b32_e32 v83, 0xffff0000, v84
	v_lshlrev_b32_e32 v84, 16, v85
	v_and_b32_e32 v85, 0xffff0000, v85
	v_lshlrev_b32_e32 v86, 16, v88
	v_and_b32_e32 v87, 0xffff0000, v88
	v_lshlrev_b32_e32 v88, 16, v89
	v_and_b32_e32 v89, 0xffff0000, v89
	v_lshlrev_b32_e32 v90, 16, v92
	v_and_b32_e32 v91, 0xffff0000, v92
	v_lshlrev_b32_e32 v92, 16, v93
	v_and_b32_e32 v93, 0xffff0000, v93
	v_lshlrev_b32_e32 v94, 16, v96
	v_and_b32_e32 v95, 0xffff0000, v96
	v_lshlrev_b32_e32 v96, 16, v97
	v_and_b32_e32 v97, 0xffff0000, v97
	v_add_u32_e32 v134, s66, v134
	v_add_u32_e32 v107, s73, v134
	v_cmp_le_i32_e32 vcc, s37, v107
	v_add_u32_e32 v106, s70, v106
	v_add_u32_e32 v143, s71, v143
	s_or_b64 s[50:51], vcc, s[50:51]
	v_add_u32_e32 v144, s71, v144
	s_waitcnt lgkmcnt(0)
	s_barrier
	s_andn2_b64 exec, exec, s[50:51]
	s_cbranch_execz .LBB0_1090

.LBB0_1048:
	s_or_b64 exec, exec, s[14:15]
	v_ashrrev_i32_e32 v115, 31, v114
	v_lshlrev_b64 v[114:115], 11, v[114:115]
	v_lshl_add_u64 v[114:115], v[102:103], 0, v[114:115]
	v_ashrrev_i32_e32 v125, 31, v124
	global_store_dwordx2 v[114:115], v[116:117], off
	global_store_dwordx2 v[114:115], v[118:119], off offset:512
	global_store_dwordx2 v[114:115], v[120:121], off offset:1024
	global_store_dwordx2 v[114:115], v[122:123], off offset:1536
	v_lshlrev_b64 v[114:115], 11, v[124:125]
	v_lshl_add_u64 v[114:115], v[102:103], 0, v[114:115]
	global_store_dwordx2 v[114:115], v[126:127], off
	global_store_dwordx2 v[114:115], v[128:129], off offset:512
	global_store_dwordx2 v[114:115], v[130:131], off offset:1024
	global_store_dwordx2 v[114:115], v[132:133], off offset:1536
	s_waitcnt lgkmcnt(0)
	s_barrier
	ds_read_b128 v[114:117], v147
	ds_read_b128 v[118:121], v147 offset:64
	s_waitcnt lgkmcnt(1)
	v_mfma_f32_16x16x32_bf16 v[122:125], v[0:3], v[114:117], 0
	ds_read_b128 v[126:129], v147 offset:33024
	ds_read_b128 v[130:133], v147 offset:33088
	s_mov_b64 s[56:57], -1
	s_mov_b64 s[14:15], -1
	v_mfma_f32_16x16x32_bf16 v[152:155], v[32:35], v[114:117], 0
	v_mfma_f32_16x16x32_bf16 v[122:125], v[4:7], v[114:117], v[122:125]
	v_mfma_f32_16x16x32_bf16 v[114:117], v[36:39], v[114:117], v[152:155]
	s_waitcnt lgkmcnt(1)
	v_mfma_f32_16x16x32_bf16 v[122:125], v[0:3], v[126:129], v[122:125]
	v_mfma_f32_16x16x32_bf16 v[114:117], v[32:35], v[126:129], v[114:117]
	v_mfma_f32_16x16x32_bf16 v[122:125], v[8:11], v[118:121], v[122:125]
	v_mfma_f32_16x16x32_bf16 v[114:117], v[40:43], v[118:121], v[114:117]
	v_mfma_f32_16x16x32_bf16 v[122:125], v[12:15], v[118:121], v[122:125]
	v_mfma_f32_16x16x32_bf16 v[114:117], v[44:47], v[118:121], v[114:117]
	ds_read_b128 v[118:121], v147 offset:128
	ds_read_b128 v[126:129], v147 offset:192
	s_waitcnt lgkmcnt(2)
	v_mfma_f32_16x16x32_bf16 v[122:125], v[8:11], v[130:133], v[122:125]
	v_mfma_f32_16x16x32_bf16 v[114:117], v[40:43], v[130:133], v[114:117]
	ds_read_b128 v[130:133], v147 offset:33152
	ds_read_b128 v[152:155], v147 offset:33216
	s_waitcnt lgkmcnt(3)
	v_mfma_f32_16x16x32_bf16 v[122:125], v[16:19], v[118:121], v[122:125]
	v_mfma_f32_16x16x32_bf16 v[114:117], v[48:51], v[118:121], v[114:117]
	v_mfma_f32_16x16x32_bf16 v[122:125], v[20:23], v[118:121], v[122:125]
	v_mfma_f32_16x16x32_bf16 v[114:117], v[52:55], v[118:121], v[114:117]
	s_waitcnt lgkmcnt(1)
	v_mfma_f32_16x16x32_bf16 v[122:125], v[16:19], v[130:133], v[122:125]
	v_mfma_f32_16x16x32_bf16 v[114:117], v[48:51], v[130:133], v[114:117]
	v_mfma_f32_16x16x32_bf16 v[118:121], v[24:27], v[126:129], v[122:125]
	v_mfma_f32_16x16x32_bf16 v[114:117], v[56:59], v[126:129], v[114:117]
	v_mfma_f32_16x16x32_bf16 v[118:121], v[28:31], v[126:129], v[118:121]
	v_mfma_f32_16x16x32_bf16 v[114:117], v[60:63], v[126:129], v[114:117]
	s_waitcnt lgkmcnt(0)
	v_mfma_f32_16x16x32_bf16 v[118:121], v[24:27], v[152:155], v[118:121]
	s_nop 7
	ds_write2_b32 v148, v118, v119 offset1:1
	ds_write2_b32 v148, v120, v121 offset0:2 offset1:3
	v_mfma_f32_16x16x32_bf16 v[114:117], v[56:59], v[152:155], v[114:117]
	s_nop 7
	ds_write2_b32 v148, v114, v115 offset0:16 offset1:17
	ds_write2_b32 v148, v116, v117 offset0:18 offset1:19
	s_waitcnt lgkmcnt(0)
	s_barrier
	ds_read_b32 v109, v149
	ds_read_b32 v111, v149 offset:2112
	ds_read_b32 v113, v149 offset:4224
	ds_read_b32 v114, v149 offset:6336
	ds_read_b32 v115, v149 offset:8448
	ds_read_b32 v116, v149 offset:10560
	ds_read_b32 v117, v149 offset:12672
	ds_read_b32 v118, v149 offset:14784
	s_waitcnt lgkmcnt(7)
	v_add_f32_e32 v107, v203, v109
	s_waitcnt lgkmcnt(6)
	v_add_f32_e32 v107, v107, v111
	s_waitcnt lgkmcnt(5)
	v_add_f32_e32 v107, v107, v113
	s_waitcnt lgkmcnt(4)
	v_add_f32_e32 v107, v107, v114
	s_waitcnt lgkmcnt(3)
	v_add_f32_e32 v107, v107, v115
	s_waitcnt lgkmcnt(2)
	v_add_f32_e32 v107, v107, v116
	s_waitcnt lgkmcnt(1)
	v_add_f32_e32 v107, v107, v117
	s_waitcnt lgkmcnt(0)
	v_add_f32_e32 v113, v107, v118
	ds_bpermute_b32 v107, v141, v113
	ds_bpermute_b32 v109, v141, v65
	s_waitcnt lgkmcnt(1)
	v_cmp_nlt_f32_e32 vcc, v113, v107
	s_and_saveexec_b64 s[58:59], vcc
	s_cbranch_execz .LBB0_1050
	v_cmp_eq_f32_e32 vcc, v113, v107
	s_waitcnt lgkmcnt(0)
	v_cmp_lt_i32_e64 s[14:15], v109, v65
	s_and_b64 s[14:15], vcc, s[14:15]
	s_orn2_b64 s[14:15], s[14:15], exec

.LBB0_2158:
	s_cmp_lt_i32 s88, 20
	s_cselect_b64 s[14:15], -1, 0
	s_and_b64 s[2:3], s[14:15], s[2:3]
	s_andn2_b64 vcc, exec, s[2:3]
	s_cbranch_vccnz .LBB0_2181
	v_mbcnt_lo_u32_b32 v0, -1, 0
	v_mbcnt_hi_u32_b32 v0, -1, v0
	v_readlane_b32 s2, v254, 0
	s_mov_b64 s[16:17], s[86:87]
	v_lshl_or_b32 v80, s96, 6, v0
	s_mov_b32 s18, s2
	s_load_dword s21, s[0:1], 0x108
	v_lshl_add_u32 v0, s18, 9, v80
	v_ashrrev_i32_e32 v74, 7, v0
	s_mov_b32 s19, 0x8800
	v_lshlrev_b32_e32 v78, 3, v80
	v_cmp_gt_i32_e32 vcc, s19, v74
	s_load_dwordx2 s[2:3], s[0:1], 0x60
	s_waitcnt lgkmcnt(0)
	s_load_dwordx2 s[8:9], s[0:1], 0x68
	s_waitcnt lgkmcnt(0)
	s_and_saveexec_b64 s[4:5], vcc
	s_cbranch_execz .LBB0_2164
	s_waitcnt vmcnt(0)
	v_and_b32_e32 v56, 0x3f8, v78
	v_mov_b32_e32 v73, 0
	v_lshlrev_b32_e32 v72, 2, v56
	v_lshl_add_u64 v[0:1], s[8:9], 0, v[72:73]
	v_add_co_u32_e32 v10, vcc, 0x1000, v0
	v_lshl_add_u64 v[24:25], s[2:3], 0, v[72:73]
	s_nop 0
	v_addc_co_u32_e32 v11, vcc, 0, v1, vcc
	v_add_co_u32_e32 v16, vcc, 0x7000, v24
	s_mov_b64 s[2:3], 0x4000
	s_nop 0
	v_addc_co_u32_e32 v17, vcc, 0, v25, vcc
	v_add_co_u32_e32 v26, vcc, 0x6000, v24
	v_lshl_add_u64 v[58:59], v[24:25], 0, s[2:3]
	s_nop 0
	v_addc_co_u32_e32 v27, vcc, 0, v25, vcc
	v_add_co_u32_e32 v32, vcc, 0x5000, v24
	s_mov_b64 s[2:3], 0x7000
	s_nop 0
	v_addc_co_u32_e32 v33, vcc, 0, v25, vcc
	v_lshl_add_u64 v[60:61], v[24:25], 0, s[2:3]
	s_mov_b64 s[2:3], 0x6000
	v_add_co_u32_e32 v34, vcc, 0x4000, v24
	s_mov_b64 s[8:9], 0x1000
	v_lshl_add_u64 v[18:19], v[24:25], 0, s[2:3]
	s_mov_b64 s[2:3], 0x5000
	v_addc_co_u32_e32 v35, vcc, 0, v25, vcc
	s_mov_b32 s22, 0x8000
	v_lshl_add_u64 v[8:9], v[0:1], 0, s[8:9]
	v_lshl_add_u64 v[28:29], v[24:25], 0, s[2:3]
	v_cmp_gt_i32_e32 vcc, s22, v74
	v_mov_b32_e32 v82, 0xff
	v_mov_b32_e32 v83, 0xfff
	global_load_dwordx4 v[0:3], v[10:11], off
	global_load_dwordx4 v[4:7], v[8:9], off offset:16
	s_nop 0
	global_load_dwordx4 v[8:11], v[16:17], off
	global_load_dwordx4 v[12:15], v[18:19], off offset:16
	s_nop 0
	global_load_dwordx4 v[16:19], v[26:27], off
	global_load_dwordx4 v[20:23], v[28:29], off offset:16
	s_nop 0
	global_load_dwordx4 v[24:27], v[32:33], off
	global_load_dwordx4 v[28:31], v[34:35], off
	v_cndmask_b32_e32 v32, v82, v83, vcc
	v_mov_b32_e32 v79, 0x100
	v_mov_b32_e32 v81, 0x1000
	v_and_b32_e32 v37, v32, v74
	s_add_u32 s6, s16, 0x17900000
	v_cndmask_b32_e32 v36, v79, v81, vcc
	v_add_u32_e32 v32, -2, v37
	s_addc_u32 s7, s17, 0
	v_add_u32_e32 v33, -2, v74
	v_cmp_lt_u32_e32 vcc, v32, v36
	s_movk_i32 s23, 0x5a00
	v_lshlrev_b32_e32 v72, 1, v56
	v_cndmask_b32_e32 v34, v74, v33, vcc
	v_mov_b64_e32 v[32:33], s[6:7]
	v_mad_i64_i32 v[34:35], s[2:3], v34, s23, v[32:33]
	s_movk_i32 s20, 0x1000
	v_lshl_add_u64 v[34:35], v[34:35], 0, v[72:73]
	v_add_co_u32_e32 v62, vcc, s20, v34
	v_add_u32_e32 v34, -1, v37
	s_nop 0
	v_addc_co_u32_e32 v63, vcc, 0, v35, vcc
	v_cmp_lt_u32_e32 vcc, v34, v36
	v_ashrrev_i32_e32 v75, 31, v74
	v_and_b32_e32 v57, 0x7f, v80
	v_subbrev_co_u32_e32 v34, vcc, 0, v74, vcc
	v_mad_i64_i32 v[34:35], s[2:3], v34, s23, v[32:33]
	v_lshl_add_u64 v[34:35], v[34:35], 0, v[72:73]
	v_add_co_u32_e32 v64, vcc, s20, v34
	s_waitcnt lgkmcnt(0)
	s_lshl_b32 s8, s21, 2
	v_addc_co_u32_e32 v65, vcc, 0, v35, vcc
	v_mad_i64_i32 v[34:35], s[2:3], v74, s23, v[32:33]
	v_lshl_add_u64 v[34:35], v[34:35], 0, v[72:73]
	v_add_co_u32_e32 v66, vcc, s20, v34
	v_add_u32_e32 v34, 1, v37
	s_nop 0
	v_addc_co_u32_e32 v67, vcc, 0, v35, vcc
	v_cmp_lt_u32_e32 vcc, v34, v36
	s_ashr_i32 s9, s8, 31
	s_lshl_b64 s[10:11], s[8:9], 11
	v_addc_co_u32_e32 v34, vcc, 0, v74, vcc
	v_mad_i64_i32 v[32:33], s[2:3], v34, s23, v[32:33]
	v_lshl_add_u64 v[32:33], v[32:33], 0, v[72:73]
	v_add_co_u32_e32 v68, vcc, s20, v32
	s_mov_b64 s[2:3], 0x6a600000
	s_nop 0
	v_addc_co_u32_e32 v69, vcc, 0, v33, vcc
	global_load_dwordx4 v[44:47], v[66:67], off offset:2048
	global_load_dwordx4 v[40:43], v[68:69], off offset:2048
	global_load_dwordx4 v[52:55], v[62:63], off offset:2048
	global_load_dwordx4 v[48:51], v[64:65], off offset:2048
	global_load_dwordx4 v[32:35], v[60:61], off offset:16
	global_load_dwordx4 v[36:39], v[58:59], off offset:16
	v_lshlrev_b64 v[58:59], 11, v[74:75]
	v_lshl_or_b32 v58, v57, 4, v58
	v_lshl_add_u64 v[58:59], s[16:17], 0, v[58:59]
	v_lshl_add_u64 v[76:77], v[58:59], 0, s[2:3]
	v_lshlrev_b32_e32 v72, 1, v56
	s_mov_b64 s[12:13], 0
	s_mov_b32 s9, 0x87ff
	s_waitcnt vmcnt(5)
	v_mov_b64_e32 v[66:67], v[46:47]
	s_waitcnt vmcnt(4)
	v_mov_b64_e32 v[70:71], v[42:43]
	s_waitcnt vmcnt(3)
	v_mov_b64_e32 v[58:59], v[54:55]
	s_waitcnt vmcnt(2)
	v_mov_b64_e32 v[62:63], v[50:51]
	v_mov_b64_e32 v[68:69], v[40:41]
	v_mov_b64_e32 v[64:65], v[44:45]
	v_mov_b64_e32 v[60:61], v[48:49]
	v_mov_b64_e32 v[56:57], v[52:53]
	s_waitcnt vmcnt(0)
	s_branch .LBB0_2162
.LBB0_2161:
	s_or_b64 exec, exec, s[2:3]
	v_cmp_gt_i32_e32 vcc, s22, v74
	v_lshlrev_b32_e32 v92, 16, v52
	v_and_b32_e32 v93, 0xffff0000, v52
	v_cndmask_b32_e32 v84, v82, v83, vcc
	v_and_b32_e32 v85, v84, v74
	v_cndmask_b32_e32 v87, v79, v81, vcc
	v_add_u32_e32 v74, -2, v85
	v_cmp_lt_u32_e32 vcc, v74, v87
	v_add_u32_e32 v84, -1, v85
	v_lshlrev_b32_e32 v94, 16, v48
	v_cndmask_b32_e64 v74, 0, 1.0, vcc
	v_cmp_lt_u32_e32 vcc, v84, v87
	v_pk_mul_f32 v[90:91], v[28:29], v[74:75] op_sel_hi:[1,0]
	v_and_b32_e32 v95, 0xffff0000, v48
	v_cndmask_b32_e64 v84, 0, 1.0, vcc
	v_cmp_lt_u32_e32 vcc, v85, v87
	v_add_u32_e32 v85, 1, v85
	v_pk_fma_f32 v[90:91], v[90:91], v[92:93], v[0:1]
	v_cndmask_b32_e64 v86, 0, 1.0, vcc
	v_cmp_lt_u32_e32 vcc, v85, v87
	v_pk_mul_f32 v[92:93], v[24:25], v[84:85] op_sel_hi:[1,0]
	v_lshlrev_b32_e32 v52, 16, v53
	v_cndmask_b32_e64 v88, 0, 1.0, vcc
	v_pk_fma_f32 v[90:91], v[92:93], v[94:95], v[90:91]
	v_pk_mul_f32 v[92:93], v[16:17], v[86:87] op_sel_hi:[1,0]
	v_lshlrev_b32_e32 v94, 16, v44
	v_and_b32_e32 v95, 0xffff0000, v44
	v_pk_fma_f32 v[90:91], v[92:93], v[94:95], v[90:91]
	v_pk_mul_f32 v[92:93], v[8:9], v[88:89] op_sel_hi:[1,0]
	v_lshlrev_b32_e32 v94, 16, v40
	v_and_b32_e32 v95, 0xffff0000, v40
	v_pk_fma_f32 v[90:91], v[92:93], v[94:95], v[90:91]
	v_pk_mul_f32 v[92:93], v[30:31], v[74:75] op_sel_hi:[1,0]
	v_and_b32_e32 v53, 0xffff0000, v53
	v_pk_fma_f32 v[52:53], v[92:93], v[52:53], v[2:3]
	v_pk_mul_f32 v[92:93], v[26:27], v[84:85] op_sel_hi:[1,0]
	v_lshlrev_b32_e32 v48, 16, v49
	v_and_b32_e32 v49, 0xffff0000, v49
	v_pk_fma_f32 v[48:49], v[92:93], v[48:49], v[52:53]
	v_pk_mul_f32 v[52:53], v[18:19], v[86:87] op_sel_hi:[1,0]
	v_lshlrev_b32_e32 v44, 16, v45
	v_and_b32_e32 v45, 0xffff0000, v45
	v_pk_fma_f32 v[44:45], v[52:53], v[44:45], v[48:49]
	v_pk_mul_f32 v[48:49], v[10:11], v[88:89] op_sel_hi:[1,0]
	v_lshlrev_b32_e32 v40, 16, v41
	v_and_b32_e32 v41, 0xffff0000, v41
	v_pk_fma_f32 v[44:45], v[48:49], v[40:41], v[44:45]
	v_pk_mul_f32 v[40:41], v[36:37], v[74:75] op_sel_hi:[1,0]
	v_lshlrev_b32_e32 v48, 16, v54
	v_and_b32_e32 v49, 0xffff0000, v54
	v_pk_fma_f32 v[40:41], v[40:41], v[48:49], v[4:5]
	v_pk_mul_f32 v[48:49], v[20:21], v[84:85] op_sel_hi:[1,0]
	v_lshlrev_b32_e32 v52, 16, v50
	v_and_b32_e32 v53, 0xffff0000, v50
	v_pk_fma_f32 v[40:41], v[48:49], v[52:53], v[40:41]
	v_pk_mul_f32 v[48:49], v[12:13], v[86:87] op_sel_hi:[1,0]
	v_lshlrev_b32_e32 v52, 16, v46
	v_and_b32_e32 v53, 0xffff0000, v46
	v_pk_fma_f32 v[40:41], v[48:49], v[52:53], v[40:41]
	v_pk_mul_f32 v[48:49], v[32:33], v[88:89] op_sel_hi:[1,0]
	v_lshlrev_b32_e32 v52, 16, v42
	v_and_b32_e32 v53, 0xffff0000, v42
	v_pk_fma_f32 v[48:49], v[48:49], v[52:53], v[40:41]
	v_pk_mul_f32 v[40:41], v[38:39], v[74:75] op_sel_hi:[1,0]
	v_lshlrev_b32_e32 v52, 16, v55
	v_and_b32_e32 v53, 0xffff0000, v55
	v_pk_fma_f32 v[40:41], v[40:41], v[52:53], v[6:7]
	v_pk_mul_f32 v[52:53], v[22:23], v[84:85] op_sel_hi:[1,0]
	v_lshlrev_b32_e32 v50, 16, v51
	v_and_b32_e32 v51, 0xffff0000, v51
	v_pk_fma_f32 v[40:41], v[52:53], v[50:51], v[40:41]
	v_pk_mul_f32 v[50:51], v[14:15], v[86:87] op_sel_hi:[1,0]
	v_lshlrev_b32_e32 v46, 16, v47
	v_and_b32_e32 v47, 0xffff0000, v47
	v_pk_fma_f32 v[40:41], v[50:51], v[46:47], v[40:41]
	v_pk_mul_f32 v[46:47], v[34:35], v[88:89] op_sel_hi:[1,0]
	v_lshlrev_b32_e32 v42, 16, v43
	v_and_b32_e32 v43, 0xffff0000, v43
	v_pk_fma_f32 v[46:47], v[46:47], v[42:43], v[40:41]
	v_cvt_pk_bf16_f32 v40, v90, v91
	v_cvt_pk_bf16_f32 v41, v44, v45
	v_cvt_pk_bf16_f32 v42, v48, v49
	v_cvt_pk_bf16_f32 v43, v46, v47
	global_store_dwordx4 v[76:77], v[40:43], off
	s_waitcnt vmcnt(1)
	v_mov_b64_e32 v[44:45], v[64:65]
	v_mov_b64_e32 v[48:49], v[60:61]
	v_mov_b64_e32 v[40:41], v[68:69]
	v_mov_b64_e32 v[52:53], v[56:57]
	v_lshl_add_u64 v[76:77], v[76:77], 0, s[10:11]
	v_mov_b64_e32 v[42:43], v[70:71]
	v_mov_b64_e32 v[46:47], v[66:67]
	v_mov_b64_e32 v[50:51], v[62:63]
	v_mov_b64_e32 v[54:55], v[58:59]
	v_mov_b32_e32 v74, v75
	s_andn2_b64 exec, exec, s[12:13]
	s_cbranch_execz .LBB0_2164
